# cross-attention: last tile's score MFMAs also read one fragment ahead; plus the ssd_local state tile stored as 8 dwordx4 through LDS (v67's change) on top of the cross-attention prefetch
# baseline (speedup 1.0000x reference)
.LBB0_1271:
	v_mov_b32_e32 v32, v209
	ds_read_b128 v[80:83], v101 offset:9216
	ds_read_b128 v[84:87], v101 offset:13824
	v_mov_b32_e32 v33, v32
	v_mov_b32_e32 v34, v32
	v_mov_b32_e32 v35, v32
	v_mov_b32_e32 v36, v32
	v_mov_b32_e32 v37, v32
	v_mov_b32_e32 v38, v32
	v_mov_b32_e32 v39, v32
	v_mov_b32_e32 v40, v32
	v_mov_b32_e32 v41, v32
	v_mov_b32_e32 v42, v32
	v_mov_b32_e32 v43, v32
	v_mov_b32_e32 v44, v32
	v_mov_b32_e32 v45, v32
	v_mov_b32_e32 v46, v32
	v_mov_b32_e32 v47, v32
	s_waitcnt lgkmcnt(1)
	s_nop 0
	v_mfma_f32_32x32x16_bf16 v[48:63], v[80:83], v[76:79], v[32:47]
	ds_read_b128 v[80:83], v101 offset:9248
	s_waitcnt lgkmcnt(1)
	v_mfma_f32_32x32x16_bf16 v[32:47], v[84:87], v[76:79], v[32:47]
	ds_read_b128 v[84:87], v101 offset:13856
	s_waitcnt lgkmcnt(1)
	v_mfma_f32_32x32x16_bf16 v[48:63], v[80:83], v[72:75], v[48:63]
	ds_read_b128 v[80:83], v101 offset:9280
	s_waitcnt lgkmcnt(1)
	v_mfma_f32_32x32x16_bf16 v[32:47], v[84:87], v[72:75], v[32:47]
	ds_read_b128 v[84:87], v101 offset:13888
	s_waitcnt lgkmcnt(1)
	v_mfma_f32_32x32x16_bf16 v[48:63], v[80:83], v[68:71], v[48:63]
	ds_read_b128 v[80:83], v101 offset:9312
	s_waitcnt lgkmcnt(1)
	v_mfma_f32_32x32x16_bf16 v[32:47], v[84:87], v[68:71], v[32:47]
	ds_read_b128 v[84:87], v101 offset:13920
	s_waitcnt lgkmcnt(1)
	v_mfma_f32_32x32x16_bf16 v[48:63], v[80:83], v[64:67], v[48:63]
	s_waitcnt lgkmcnt(0)
	v_mfma_f32_32x32x16_bf16 v[32:47], v[84:87], v[64:67], v[32:47]
	s_nop 8
	v_max_f32_e32 v72, v49, v49
	v_max_f32_e32 v73, v48, v48
	v_max_f32_e32 v72, v73, v72
	v_max3_f32 v64, v50, v51, v33
	v_max3_f32 v65, v72, v32, v34
	v_max3_f32 v65, v65, v35, v52
	v_max3_f32 v64, v64, v54, v55
	v_max3_f32 v65, v65, v53, v36
	v_max3_f32 v64, v64, v38, v39
	v_max3_f32 v65, v65, v37, v56
	v_max3_f32 v64, v64, v58, v59
	v_max3_f32 v65, v65, v57, v40
	v_max3_f32 v64, v64, v42, v43
	v_max3_f32 v65, v65, v41, v60
	v_max3_f32 v64, v64, v62, v63
	v_max3_f32 v65, v65, v61, v44
	v_max3_f32 v64, v64, v46, v47
	v_max3_f32 v64, v65, v45, v64
	ds_bpermute_b32 v65, v102, v64
	s_waitcnt lgkmcnt(0)
	v_max_f32_e32 v65, v65, v65
	v_max_f32_e32 v64, v64, v65
	v_add_f32_e32 v64, 0, v64
	v_max_f32_e32 v65, v100, v100
	v_max_f32_e32 v72, v65, v64
	v_sub_f32_e32 v48, v48, v72
	v_exp_f32_e32 v64, v48
	v_sub_f32_e32 v48, v49, v72
	v_exp_f32_e32 v65, v48
	v_sub_f32_e32 v50, v50, v72
	v_exp_f32_e32 v66, v50
	v_sub_f32_e32 v50, v51, v72
	v_sub_f32_e32 v32, v32, v72
	v_exp_f32_e32 v67, v50
	v_sub_f32_e32 v33, v33, v72
	v_exp_f32_e32 v32, v32
	v_add_f32_e32 v48, 0, v64
	v_exp_f32_e32 v33, v33
	v_add_f32_e32 v48, v65, v48
	v_sub_f32_e32 v34, v34, v72
	v_exp_f32_e32 v34, v34
	v_sub_f32_e32 v35, v35, v72
	v_add_f32_e32 v48, v66, v48
	v_exp_f32_e32 v35, v35
	v_add_f32_e32 v50, v67, v48
	v_sub_f32_e32 v48, v52, v72
	v_sub_f32_e32 v36, v36, v72
	v_add_f32_e32 v49, 0, v32
	v_exp_f32_e32 v68, v48
	v_exp_f32_e32 v36, v36
	v_sub_f32_e32 v48, v53, v72
	v_sub_f32_e32 v37, v37, v72
	v_add_f32_e32 v49, v33, v49
	v_exp_f32_e32 v69, v48
	v_exp_f32_e32 v48, v37
	v_add_f32_e32 v49, v34, v49
	v_add_f32_e32 v49, v35, v49
	v_add_f32_e32 v49, v36, v49
	v_add_f32_e32 v37, v68, v50
	v_add_f32_e32 v50, v48, v49
	v_sub_f32_e32 v49, v54, v72
	v_exp_f32_e32 v70, v49
	v_sub_f32_e32 v38, v38, v72
	v_sub_f32_e32 v49, v55, v72
	v_exp_f32_e32 v38, v38
	v_exp_f32_e32 v71, v49
	v_sub_f32_e32 v39, v39, v72
	v_exp_f32_e32 v49, v39
	v_add_f32_e32 v37, v69, v37
	v_add_f32_e32 v37, v70, v37
	v_add_f32_e32 v39, v38, v50
	v_add_f32_e32 v50, v71, v37
	v_sub_f32_e32 v37, v56, v72
	v_add_f32_e32 v53, v49, v39
	v_exp_f32_e32 v51, v37
	v_sub_f32_e32 v37, v40, v72
	v_sub_f32_e32 v39, v57, v72
	v_exp_f32_e32 v37, v37
	v_exp_f32_e32 v52, v39
	v_sub_f32_e32 v39, v41, v72
	v_exp_f32_e32 v39, v39
	v_add_f32_e32 v41, v37, v53
	v_add_f32_e32 v40, v51, v50
	v_add_f32_e32 v40, v52, v40
	v_add_f32_e32 v55, v39, v41
	v_sub_f32_e32 v41, v58, v72
	v_exp_f32_e32 v53, v41
	v_sub_f32_e32 v41, v42, v72
	v_exp_f32_e32 v41, v41
	v_sub_f32_e32 v42, v59, v72
	v_exp_f32_e32 v54, v42
	v_sub_f32_e32 v42, v43, v72
	v_sub_f32_e32 v43, v60, v72
	v_exp_f32_e32 v50, v42
	v_add_f32_e32 v42, v41, v55
	v_exp_f32_e32 v55, v43
	v_sub_f32_e32 v43, v44, v72
	v_exp_f32_e32 v44, v43
	v_sub_f32_e32 v43, v61, v72
	v_exp_f32_e32 v56, v43
	v_sub_f32_e32 v43, v45, v72
	v_exp_f32_e32 v45, v43
	v_sub_f32_e32 v43, v62, v72
	v_exp_f32_e32 v57, v43
	v_sub_f32_e32 v43, v46, v72
	v_exp_f32_e32 v46, v43
	v_sub_f32_e32 v43, v63, v72
	v_add_f32_e32 v40, v53, v40
	v_exp_f32_e32 v58, v43
	v_sub_f32_e32 v43, v47, v72
	v_add_f32_e32 v40, v54, v40
	v_add_f32_e32 v42, v50, v42
	v_exp_f32_e32 v47, v43
	v_add_f32_e32 v40, v55, v40
	v_add_f32_e32 v42, v44, v42
	v_add_f32_e32 v40, v56, v40
	v_add_f32_e32 v42, v45, v42
	v_add_f32_e32 v40, v57, v40
	v_add_f32_e32 v42, v46, v42
	v_add_f32_e32 v43, v58, v40
	v_add_f32_e32 v42, v47, v42
	v_sub_f32_e32 v73, v100, v72
	v_add_f32_e32 v42, v43, v42
	v_exp_f32_e32 v40, v73
	ds_bpermute_b32 v43, v102, v42
	v_cmp_neq_f32_e32 vcc, 1.0, v40
	s_cbranch_vccz .LBB0_1273
	ds_write_b32 v98, v40 offset:43008
	ds_read_b128 v[60:63], v97 offset:43104
	ds_read_b128 v[72:75], v97 offset:43072
	ds_read_b128 v[76:79], v97 offset:43040
	ds_read_b128 v[80:83], v97 offset:43008
	s_waitcnt lgkmcnt(3)
	v_pk_mul_f32 v[14:15], v[14:15], v[62:63]
	s_waitcnt lgkmcnt(2)
	v_pk_mul_f32 v[10:11], v[10:11], v[74:75]
	s_waitcnt lgkmcnt(1)
	v_pk_mul_f32 v[6:7], v[6:7], v[78:79]
	s_waitcnt lgkmcnt(0)
	v_pk_mul_f32 v[2:3], v[2:3], v[82:83]
	v_pk_mul_f32 v[12:13], v[12:13], v[60:61]
	v_pk_mul_f32 v[8:9], v[8:9], v[72:73]
	v_pk_mul_f32 v[4:5], v[4:5], v[76:77]
	v_pk_mul_f32 v[0:1], v[0:1], v[80:81]
	v_pk_mul_f32 v[30:31], v[30:31], v[62:63]
	v_pk_mul_f32 v[26:27], v[26:27], v[74:75]
	v_pk_mul_f32 v[22:23], v[22:23], v[78:79]
	v_pk_mul_f32 v[18:19], v[18:19], v[82:83]
	v_pk_mul_f32 v[28:29], v[28:29], v[60:61]
	v_pk_mul_f32 v[24:25], v[24:25], v[72:73]
	v_pk_mul_f32 v[20:21], v[20:21], v[76:77]
	v_pk_mul_f32 v[16:17], v[16:17], v[80:81]
